# v3 + P4 elem-first waves issue the chunk c+2 operand loads after the MFMA part instead of before it
# baseline (speedup 1.0000x reference)
.LBB0_413:
	s_or_b64 exec, exec, s[0:1]
	v_mul_u32_u24_e32 v0, 0x110, v0
	v_add3_u32 v0, s39, v0, v166
	v_cvt_pk_bf16_f32 v10, v144, v145
	s_waitcnt lgkmcnt(0)
	v_cvt_pk_bf16_f32 v11, v146, v147
	v_cvt_pk_bf16_f32 v12, v148, v149
	v_cvt_pk_bf16_f32 v13, v150, v151
	ds_write2_b64 v0, v[10:11], v[12:13] offset1:2
	v_cvt_pk_bf16_f32 v10, v152, v153
	v_cvt_pk_bf16_f32 v11, v154, v155
	v_cvt_pk_bf16_f32 v12, v156, v157
	v_cvt_pk_bf16_f32 v13, v158, v159
	ds_write2_b64 v0, v[10:11], v[12:13] offset0:4 offset1:6
	s_cmp_gt_u32 s74, 5
	s_cbranch_scc1 .Lp4y_noload
	v_lshlrev_b32_e32 v144, 4, v214
	v_and_b32_e32 v146, 3, v214
	v_and_b32_e32 v144, 0xffffffc0, v144
	v_ashrrev_i32_e32 v145, 31, v144
	v_lshlrev_b64 v[144:145], 1, v[144:145]
	s_add_u32 s0, s75, s22
	v_lshl_or_b32 v144, v146, 5, v144
	s_addc_u32 s1, s77, s23
	v_lshl_add_u64 v[148:149], s[0:1], 0, v[144:145]
	v_add_co_u32_e32 v150, vcc, s65, v148
	v_lshl_add_u64 v[144:145], v[148:149], 0, s[14:15]
	s_nop 0
	v_addc_co_u32_e32 v151, vcc, 0, v149, vcc
	v_lshl_add_u64 v[152:153], v[148:149], 0, s[16:17]
	v_add_co_u32_e32 v148, vcc, s66, v148
	v_mov_b32_e32 v154, v214
	v_ashrrev_i32_e32 v155, 31, v154
	v_addc_co_u32_e32 v149, vcc, 0, v149, vcc
	global_load_dwordx4 v[180:183], v[150:151], off
	global_load_dwordx4 v[188:191], v[144:145], off offset:16
	global_load_dwordx4 v[192:195], v[148:149], off
	global_load_dwordx4 v[184:187], v[152:153], off offset:16
	v_lshl_add_u64 v[148:149], v[154:155], 4, s[0:1]
	v_add_co_u32_e32 v152, vcc, 0x26240000, v148
	s_nop 1
	v_addc_co_u32_e32 v153, vcc, 0, v149, vcc
	v_add_co_u32_e32 v148, vcc, 0x26242000, v148
	s_nop 1
	v_addc_co_u32_e32 v149, vcc, 0, v149, vcc
	global_load_dwordx4 v[200:203], v[152:153], off
	global_load_dwordx4 v[196:199], v[148:149], off
.Lp4y_noload:
.LBB0_414:
	s_waitcnt lgkmcnt(0)
	s_waitcnt lgkmcnt(0)
	s_barrier
	global_load_dwordx4 v[10:13], v[204:205], off
	global_load_dwordx4 v[16:19], v[204:205], off offset:16
	global_load_dwordx4 v[20:23], v[204:205], off offset:32
	global_load_dwordx4 v[24:27], v[204:205], off offset:48
	v_lshl_add_u32 v0, v212, 2, 0
	v_mad_u64_u32 v[28:29], s[0:1], v212, s64, v[14:15]
	s_waitcnt vmcnt(5)
	v_lshlrev_b32_e32 v30, 16, v6
	v_and_b32_e32 v31, 0xffff0000, v6
	v_lshlrev_b32_e32 v32, 16, v7
	v_and_b32_e32 v33, 0xffff0000, v7
	v_lshlrev_b32_e32 v34, 16, v8
	v_and_b32_e32 v35, 0xffff0000, v8
	v_lshlrev_b32_e32 v36, 16, v9
	v_and_b32_e32 v37, 0xffff0000, v9
	s_waitcnt vmcnt(4)
	v_lshlrev_b32_e32 v38, 16, v2
	v_and_b32_e32 v39, 0xffff0000, v2
	v_lshlrev_b32_e32 v40, 16, v3
	v_and_b32_e32 v41, 0xffff0000, v3
	v_lshlrev_b32_e32 v42, 16, v4
	v_and_b32_e32 v43, 0xffff0000, v4
	v_lshlrev_b32_e32 v44, 16, v5
	v_and_b32_e32 v45, 0xffff0000, v5
	ds_read_b128 v[2:5], v28
	v_add_u32_e32 v0, 0x27800, v0
	ds_read_b128 v[6:9], v28 offset:16
	ds_read2st64_b32 v[28:29], v0 offset1:1
	ds_read2st64_b32 v[46:47], v0 offset0:2 offset1:3
	s_add_i32 s74, s74, 1
	s_add_u32 s22, s22, 0x20000
	s_waitcnt lgkmcnt(3)
	v_lshlrev_b32_e32 v48, 16, v2
	s_waitcnt lgkmcnt(1)
	v_mov_b32_e32 v56, v28
	s_waitcnt lgkmcnt(0)
	v_mov_b32_e32 v57, v46
	v_mov_b32_e32 v46, v29
	v_pk_add_f32 v[28:29], v[56:57], v[46:47]
	v_and_b32_e32 v49, 0xffff0000, v2
	v_add_f32_e32 v0, v28, v29
	v_fmamk_f32 v0, v0, 0x3c000000, v219
	v_rsq_f32_e32 v0, v0
	v_lshlrev_b32_e32 v2, 16, v3
	v_and_b32_e32 v3, 0xffff0000, v3
	v_lshlrev_b32_e32 v50, 16, v4
	v_and_b32_e32 v51, 0xffff0000, v4
	v_lshlrev_b32_e32 v4, 16, v5
	v_and_b32_e32 v5, 0xffff0000, v5
	v_lshlrev_b32_e32 v52, 16, v6
	v_and_b32_e32 v53, 0xffff0000, v6
	v_lshlrev_b32_e32 v6, 16, v7
	v_and_b32_e32 v7, 0xffff0000, v7
	v_pk_mul_f32 v[2:3], v[0:1], v[2:3] op_sel_hi:[0,1]
	v_pk_mul_f32 v[28:29], v[0:1], v[48:49] op_sel_hi:[0,1]
	v_pk_mul_f32 v[4:5], v[0:1], v[4:5] op_sel_hi:[0,1]
	v_pk_mul_f32 v[46:47], v[0:1], v[50:51] op_sel_hi:[0,1]
	v_pk_mul_f32 v[6:7], v[0:1], v[6:7] op_sel_hi:[0,1]
	v_pk_mul_f32 v[48:49], v[0:1], v[52:53] op_sel_hi:[0,1]
	v_lshlrev_b32_e32 v54, 16, v8
	v_and_b32_e32 v55, 0xffff0000, v8
	v_lshlrev_b32_e32 v8, 16, v9
	v_and_b32_e32 v9, 0xffff0000, v9
	v_pk_mul_f32 v[8:9], v[0:1], v[8:9] op_sel_hi:[0,1]
	v_pk_mul_f32 v[50:51], v[0:1], v[54:55] op_sel_hi:[0,1]
	s_addc_u32 s23, s23, 0
	v_mov_b64_e32 v[64:65], v[80:81]
	v_mov_b64_e32 v[160:161], v[180:181]
	v_mov_b64_e32 v[176:177], v[196:197]
	v_mov_b64_e32 v[172:173], v[200:201]
	v_mov_b64_e32 v[168:169], v[184:185]
	v_mov_b64_e32 v[164:165], v[192:193]
	s_cmp_eq_u32 s22, 0x100000
	v_mov_b64_e32 v[66:67], v[82:83]
	v_mov_b64_e32 v[68:69], v[84:85]
	v_mov_b64_e32 v[70:71], v[86:87]
	v_mov_b64_e32 v[72:73], v[88:89]
	v_mov_b64_e32 v[74:75], v[90:91]
	v_mov_b64_e32 v[76:77], v[92:93]
	v_mov_b64_e32 v[78:79], v[94:95]
	v_mov_b64_e32 v[162:163], v[182:183]
	v_mov_b64_e32 v[178:179], v[198:199]
	v_mov_b64_e32 v[174:175], v[202:203]
	v_mov_b64_e32 v[170:171], v[186:187]
	v_mov_b64_e32 v[166:167], v[194:195]
	s_waitcnt vmcnt(3)
	v_pk_mul_f32 v[10:11], v[10:11], v[28:29]
	v_pk_mul_f32 v[2:3], v[12:13], v[2:3]
	s_waitcnt vmcnt(2)
	v_pk_mul_f32 v[12:13], v[16:17], v[46:47]
	v_pk_mul_f32 v[4:5], v[18:19], v[4:5]
	s_waitcnt vmcnt(1)
	v_pk_mul_f32 v[16:17], v[20:21], v[48:49]
	v_pk_mul_f32 v[6:7], v[22:23], v[6:7]
	v_pk_mul_f32 v[20:21], v[2:3], v[32:33]
	v_pk_mul_f32 v[2:3], v[10:11], v[30:31]
	v_pk_mul_f32 v[10:11], v[4:5], v[36:37]
	v_pk_mul_f32 v[4:5], v[12:13], v[34:35]
	v_pk_mul_f32 v[6:7], v[6:7], v[40:41]
	v_cvt_pk_bf16_f32 v2, v2, v3
	v_cvt_pk_bf16_f32 v3, v20, v21
	v_pk_mul_f32 v[12:13], v[16:17], v[38:39]
	v_cvt_pk_bf16_f32 v4, v4, v5
	v_cvt_pk_bf16_f32 v5, v10, v11
	global_store_dwordx4 v[210:211], v[2:5], off
	s_waitcnt vmcnt(1)
	v_pk_mul_f32 v[18:19], v[24:25], v[50:51]
	v_pk_mul_f32 v[8:9], v[26:27], v[8:9]
	v_cvt_pk_bf16_f32 v2, v12, v13
	v_cvt_pk_bf16_f32 v3, v6, v7
	v_add_co_u32_e32 v6, vcc, s61, v208
	v_pk_mul_f32 v[8:9], v[8:9], v[44:45]
	s_nop 0
	v_addc_co_u32_e32 v7, vcc, 0, v209, vcc
	v_pk_mul_f32 v[16:17], v[18:19], v[42:43]
	v_mov_b64_e32 v[48:49], v[128:129]
	v_cvt_pk_bf16_f32 v4, v16, v17
	v_cvt_pk_bf16_f32 v5, v8, v9
	global_store_dwordx4 v[6:7], v[2:5], off offset:16
	s_waitcnt lgkmcnt(0)
	v_mov_b64_e32 v[32:33], v[112:113]
	v_mov_b64_e32 v[16:17], v[96:97]
	v_mov_b64_e32 v[10:11], v[188:189]
	v_mov_b64_e32 v[50:51], v[130:131]
	v_mov_b64_e32 v[52:53], v[132:133]
	v_mov_b64_e32 v[54:55], v[134:135]
	v_mov_b64_e32 v[56:57], v[136:137]
	v_mov_b64_e32 v[58:59], v[138:139]
	v_mov_b64_e32 v[60:61], v[140:141]
	v_mov_b64_e32 v[62:63], v[142:143]
	v_mov_b64_e32 v[34:35], v[114:115]
	v_mov_b64_e32 v[36:37], v[116:117]
	v_mov_b64_e32 v[38:39], v[118:119]
	v_mov_b64_e32 v[40:41], v[120:121]
	v_mov_b64_e32 v[42:43], v[122:123]
	v_mov_b64_e32 v[44:45], v[124:125]
	v_mov_b64_e32 v[46:47], v[126:127]
	v_mov_b64_e32 v[18:19], v[98:99]
	v_mov_b64_e32 v[20:21], v[100:101]
	v_mov_b64_e32 v[22:23], v[102:103]
	v_mov_b64_e32 v[24:25], v[104:105]
	v_mov_b64_e32 v[26:27], v[106:107]
	v_mov_b64_e32 v[28:29], v[108:109]
	v_mov_b64_e32 v[30:31], v[110:111]
	v_mov_b64_e32 v[12:13], v[190:191]
	s_barrier
	s_cbranch_scc1 .LBB0_406

.LBB0_433:
	s_or_b64 exec, exec, s[0:1]
	v_lshrrev_b32_e32 v80, 3, v84
	v_mul_lo_u32 v81, v80, s60
	v_lshlrev_b32_e32 v80, 4, v84
	v_and_b32_e32 v82, 0x70, v80
	v_add3_u32 v81, s78, v81, v82
	s_cmp_gt_u32 s74, 5
	s_waitcnt vmcnt(3)
	ds_write_b128 v81, v[172:175] offset:53248
	s_waitcnt vmcnt(2)
	ds_write_b128 v81, v[176:179] offset:62464
.LBB0_435:
	v_mov_b32_e32 v0, v214
	v_and_b32_e32 v164, 31, v0
	v_bfe_u32 v165, v0, 5, 1
	v_or_b32_e32 v0, s37, v164
	v_mov_b32_e32 v10, s76
	v_mad_u32_u24 v135, v0, s64, v10
	v_lshlrev_b32_e32 v133, 4, v165
	v_add_u32_e32 v10, v135, v133
	ds_read_b128 v[120:123], v10
	ds_read_b128 v[116:119], v10 offset:32
	ds_read_b128 v[112:115], v10 offset:64
	ds_read_b128 v[108:111], v10 offset:96
	ds_read_b128 v[104:107], v10 offset:128
	ds_read_b128 v[100:103], v10 offset:160
	ds_read_b128 v[96:99], v10 offset:192
	ds_read_b128 v[10:13], v10 offset:224
	v_or_b32_e32 v80, s8, v164
	v_mul_lo_u32 v80, v80, s60
	v_add_u32_e32 v134, s76, v80
	v_lshlrev_b32_e32 v166, 3, v165
	v_add_u32_e32 v132, s76, v133
	v_add_u32_e32 v124, v134, v166
	s_mov_b64 s[0:1], -1
	s_and_b64 vcc, exec, s[10:11]
	s_cbranch_vccz .LBB0_443
	v_mad_u32_u24 v84, v164, s64, v132
	ds_read_b128 v[80:83], v84 offset:17408
	ds_read_b128 v[126:129], v84 offset:17440
	ds_read_b128 v[136:139], v84 offset:17472
	ds_read_b128 v[140:143], v84 offset:17504
	ds_read_b128 v[144:147], v84 offset:17536
	ds_read_b128 v[148:151], v84 offset:17568
	ds_read_b128 v[152:155], v84 offset:17600
	ds_read_b128 v[156:159], v84 offset:17632
	v_add_u32_e32 v84, 0xd000, v124
	ds_read2_b64 v[160:163], v84 offset1:2
	ds_read2_b64 v[168:171], v84 offset0:4 offset1:6
	s_waitcnt lgkmcnt(0)
	s_waitcnt lgkmcnt(9)
	v_mfma_f32_32x32x16_bf16 v[80:95], v[80:83], v[120:123], 0
	s_waitcnt lgkmcnt(8)
	v_mfma_f32_32x32x16_bf16 v[80:95], v[126:129], v[116:119], v[80:95]
	s_waitcnt lgkmcnt(7)
	v_mfma_f32_32x32x16_bf16 v[80:95], v[136:139], v[112:115], v[80:95]
	s_waitcnt lgkmcnt(6)
	v_mfma_f32_32x32x16_bf16 v[80:95], v[140:143], v[108:111], v[80:95]
	s_waitcnt lgkmcnt(5)
	v_mfma_f32_32x32x16_bf16 v[80:95], v[144:147], v[104:107], v[80:95]
	s_waitcnt lgkmcnt(4)
	v_mfma_f32_32x32x16_bf16 v[80:95], v[148:151], v[100:103], v[80:95]
	s_waitcnt lgkmcnt(3)
	v_mfma_f32_32x32x16_bf16 v[80:95], v[152:155], v[96:99], v[80:95]
	s_waitcnt lgkmcnt(2)
	v_mfma_f32_32x32x16_bf16 v[80:95], v[156:159], v[10:13], v[80:95]
	s_nop 11
	v_cvt_pk_bf16_f32 v80, v80, v81
	v_cvt_pk_bf16_f32 v81, v82, v83
	v_cvt_pk_bf16_f32 v82, v84, v85
	v_cvt_pk_bf16_f32 v83, v86, v87
	s_waitcnt lgkmcnt(1)
	s_nop 0
	v_mfma_f32_32x32x16_bf16 v[144:159], v[160:163], v[80:83], 0
	v_cvt_pk_bf16_f32 v80, v88, v89
	v_cvt_pk_bf16_f32 v81, v90, v91
	v_cvt_pk_bf16_f32 v82, v92, v93
	v_cvt_pk_bf16_f32 v83, v94, v95
	s_waitcnt lgkmcnt(0)
	s_nop 0
	v_mfma_f32_32x32x16_bf16 v[144:159], v[168:171], v[80:83], v[144:159]
	s_mov_b32 s0, 1
	s_cbranch_execnz .LBB0_438
